# opt2 + scanA stage-L and rwkv_post MFMA-chain LDS reads hoisted behind single waits
# speedup vs baseline: 1.0086x; 1.0086x over previous
.LBB0_544:
	v_and_b32_e32 v40, 15, v112
	v_and_b32_e32 v75, -16, v112
	v_mul_u32_u24_e32 v95, 0x90, v40
	v_add3_u32 v41, s85, v75, v95
	ds_read_b128 v[8:11], v41
	ds_read_b128 v[12:15], v41 offset:64
	ds_read_b128 v[16:19], v41 offset:2304
	ds_read_b128 v[36:39], v41 offset:2368
	ds_read_b128 v[76:79], v41 offset:4608
	s_waitcnt lgkmcnt(4)
	v_mfma_f32_16x16x32_bf16 v[8:11], v[8:11], v[0:3], 0
	s_mul_i32 s44, s35, 0x44
	s_lshr_b32 s35, s35, 5
	s_sub_i32 s44, s78, s44
	s_waitcnt lgkmcnt(2)
	v_mfma_f32_16x16x32_bf16 v[16:19], v[16:19], v[0:3], 0
	s_cmp_eq_u32 s16, 0
	v_or_b32_e32 v99, s53, v40
	s_cselect_b64 vcc, -1, 0
	v_mfma_f32_16x16x32_bf16 v[20:23], v[12:15], v[4:7], v[8:11]
	s_cmp_lt_i32 s44, 4
	s_movk_i32 s5, 0x11ff
	v_lshl_or_b32 v42, s44, 6, v99
	ds_read_b128 v[8:11], v41 offset:4672
	s_waitcnt lgkmcnt(2)
	v_mfma_f32_16x16x32_bf16 v[16:19], v[36:39], v[4:7], v[16:19]
	ds_read_b128 v[36:39], v41 offset:6912
	s_cselect_b32 s44, 0xff, s5
	v_ashrrev_i32_e32 v44, 4, v112
	s_waitcnt lgkmcnt(2)
	v_mfma_f32_16x16x32_bf16 v[12:15], v[76:79], v[0:3], 0
	ds_read_b128 v[78:81], v41 offset:6976
	v_sub_u32_e32 v41, s44, v42
	s_mulk_i32 s35, 0x1100
	s_waitcnt lgkmcnt(2)
	v_mfma_f32_16x16x32_bf16 v[12:15], v[8:11], v[4:7], v[12:15]
	v_lshlrev_b32_e32 v98, 3, v44
	s_movk_i32 s5, 0x90
	s_mov_b64 s[44:45], -1
	s_waitcnt lgkmcnt(1)
	v_mfma_f32_16x16x32_bf16 v[8:11], v[36:39], v[0:3], 0
	v_cndmask_b32_e32 v36, v41, v42, vcc
	v_add_u32_e32 v76, s35, v36
	v_ashrrev_i32_e32 v77, 31, v76
	s_waitcnt lgkmcnt(0)
	v_mfma_f32_16x16x32_bf16 v[8:11], v[78:81], v[4:7], v[8:11]
	v_mad_u32_u24 v79, v99, s5, v98
	s_andn2_b64 vcc, exec, s[18:19]
	s_mulk_i32 s16, 0x4400
	s_cbranch_vccnz .LBB0_548
	v_lshl_add_u32 v218, v44, 4, 0
	v_add_u32_e32 v219, 0x22600, v218
	v_add_u32_e32 v220, 0x22700, v218
	ds_read_b128 v[156:159], v219
	ds_read_b128 v[160:163], v220
	v_add_u32_e32 v221, 0x22800, v218
	ds_read_b128 v[164:167], v221
	ds_read_b128 v[168:171], v219 offset:64
	ds_read_b128 v[172:175], v220 offset:64
	ds_read_b128 v[176:179], v221 offset:64
	ds_read_b128 v[180:183], v219 offset:128
	ds_read_b128 v[184:187], v220 offset:128
	ds_read_b128 v[188:191], v221 offset:128
	ds_read_b128 v[192:195], v219 offset:192
	ds_read_b128 v[210:213], v220 offset:192
	ds_read_b128 v[214:217], v221 offset:192
	v_lshl_add_u32 v42, v44, 4, 0
	v_add_u32_e32 v36, 0, v79
	v_add_u32_e32 v41, 0x18c00, v36
	v_add_u32_e32 v45, 0x1b000, v36
	v_lshlrev_b32_e32 v42, 16, v50
	s_waitcnt lgkmcnt(0)
	v_add_f32_e32 v36, v20, v156
	v_add_f32_e32 v37, v21, v157
	v_mul_f32_e32 v36, 0xbfb8aa3b, v36
	v_mul_f32_e32 v37, 0xbfb8aa3b, v37
	v_exp_f32_e32 v36, v36
	v_exp_f32_e32 v37, v37
	v_add_f32_e32 v38, v22, v158
	v_add_f32_e32 v39, v23, v159
	v_add_f32_e32 v36, 1.0, v36
	v_add_f32_e32 v37, 1.0, v37
	v_mul_f32_e32 v38, 0xbfb8aa3b, v38
	v_mul_f32_e32 v39, 0xbfb8aa3b, v39
	v_rcp_f32_e32 v36, v36
	v_rcp_f32_e32 v37, v37
	v_exp_f32_e32 v38, v38
	v_exp_f32_e32 v39, v39
	v_and_b32_e32 v43, 0xffff0000, v50
	v_pk_add_f32 v[46:47], v[36:37], -1.0 op_sel_hi:[1,0]
	v_add_f32_e32 v38, 1.0, v38
	v_add_f32_e32 v39, 1.0, v39
	v_pk_fma_f32 v[46:47], v[160:161], v[46:47], 1.0 op_sel_hi:[1,1,0]
	v_rcp_f32_e32 v38, v38
	v_rcp_f32_e32 v39, v39
	v_lshlrev_b32_e32 v105, 16, v66
	v_pk_mul_f32 v[42:43], v[46:47], v[42:43]
	v_and_b32_e32 v106, 0xffff0000, v66
	v_mul_f32_e32 v46, v42, v105
	v_fma_f32 v105, v164, v46, 0
	v_lshlrev_b32_e32 v46, 16, v58
	v_and_b32_e32 v47, 0xffff0000, v58
	v_pk_mul_f32 v[36:37], v[36:37], v[46:47]
	v_mul_f32_e32 v46, v43, v106
	v_pk_add_f32 v[80:81], v[38:39], -1.0 op_sel_hi:[1,0]
	v_fmac_f32_e32 v105, v165, v46
	v_lshlrev_b32_e32 v46, 16, v51
	v_and_b32_e32 v47, 0xffff0000, v51
	v_pk_fma_f32 v[80:81], v[162:163], v[80:81], 1.0 op_sel_hi:[1,1,0]
	v_lshlrev_b32_e32 v107, 16, v67
	v_pk_mul_f32 v[46:47], v[80:81], v[46:47]
	v_and_b32_e32 v81, 0xffff0000, v59
	v_mul_f32_e32 v80, v46, v107
	v_fmac_f32_e32 v105, v166, v80
	v_lshlrev_b32_e32 v80, 16, v59
	v_pk_mul_f32 v[38:39], v[38:39], v[80:81]
	v_and_b32_e32 v108, 0xffff0000, v67
	v_cvt_pk_bf16_f32 v42, v42, v43
	v_cvt_pk_bf16_f32 v43, v46, v47
	v_cvt_pk_bf16_f32 v36, v36, v37
	v_cvt_pk_bf16_f32 v37, v38, v39
	v_mul_f32_e32 v80, v47, v108
	ds_write_b64 v41, v[42:43]
	ds_write_b64 v45, v[36:37]
	v_fmac_f32_e32 v105, v167, v80
	v_lshlrev_b32_e32 v42, 16, v52
	v_and_b32_e32 v43, 0xffff0000, v52
	v_add_f32_e32 v36, v16, v168
	v_add_f32_e32 v37, v17, v169
	v_mul_f32_e32 v36, 0xbfb8aa3b, v36
	v_mul_f32_e32 v37, 0xbfb8aa3b, v37
	v_exp_f32_e32 v36, v36
	v_exp_f32_e32 v37, v37
	v_add_f32_e32 v38, v18, v170
	v_add_f32_e32 v39, v19, v171
	v_add_f32_e32 v36, 1.0, v36
	v_add_f32_e32 v37, 1.0, v37
	v_mul_f32_e32 v38, 0xbfb8aa3b, v38
	v_mul_f32_e32 v39, 0xbfb8aa3b, v39
	v_rcp_f32_e32 v36, v36
	v_rcp_f32_e32 v37, v37
	v_exp_f32_e32 v38, v38
	v_exp_f32_e32 v39, v39
	v_lshlrev_b32_e32 v106, 16, v68
	v_pk_add_f32 v[46:47], v[36:37], -1.0 op_sel_hi:[1,0]
	v_add_f32_e32 v38, 1.0, v38
	v_add_f32_e32 v39, 1.0, v39
	v_pk_fma_f32 v[46:47], v[172:173], v[46:47], 1.0 op_sel_hi:[1,1,0]
	v_rcp_f32_e32 v38, v38
	v_rcp_f32_e32 v39, v39
	v_pk_mul_f32 v[42:43], v[46:47], v[42:43]
	v_and_b32_e32 v107, 0xffff0000, v68
	v_mul_f32_e32 v46, v42, v106
	v_fmac_f32_e32 v105, v176, v46
	v_lshlrev_b32_e32 v46, 16, v60
	v_and_b32_e32 v47, 0xffff0000, v60
	v_pk_mul_f32 v[36:37], v[36:37], v[46:47]
	v_mul_f32_e32 v46, v43, v107
	v_pk_add_f32 v[80:81], v[38:39], -1.0 op_sel_hi:[1,0]
	v_fmac_f32_e32 v105, v177, v46
	v_lshlrev_b32_e32 v46, 16, v53
	v_and_b32_e32 v47, 0xffff0000, v53
	v_pk_fma_f32 v[80:81], v[174:175], v[80:81], 1.0 op_sel_hi:[1,1,0]
	v_lshlrev_b32_e32 v108, 16, v69
	v_pk_mul_f32 v[46:47], v[80:81], v[46:47]
	v_and_b32_e32 v81, 0xffff0000, v61
	v_mul_f32_e32 v80, v46, v108
	v_fmac_f32_e32 v105, v178, v80
	v_lshlrev_b32_e32 v80, 16, v61
	v_pk_mul_f32 v[38:39], v[38:39], v[80:81]
	v_and_b32_e32 v109, 0xffff0000, v69
	v_cvt_pk_bf16_f32 v42, v42, v43
	v_cvt_pk_bf16_f32 v43, v46, v47
	v_cvt_pk_bf16_f32 v36, v36, v37
	v_cvt_pk_bf16_f32 v37, v38, v39
	v_mul_f32_e32 v80, v47, v109
	ds_write_b64 v41, v[42:43] offset:32
	ds_write_b64 v45, v[36:37] offset:32
	v_fmac_f32_e32 v105, v179, v80
	v_lshlrev_b32_e32 v42, 16, v54
	v_and_b32_e32 v43, 0xffff0000, v54
	v_add_f32_e32 v36, v12, v180
	v_add_f32_e32 v37, v13, v181
	v_mul_f32_e32 v36, 0xbfb8aa3b, v36
	v_mul_f32_e32 v37, 0xbfb8aa3b, v37
	v_exp_f32_e32 v36, v36
	v_exp_f32_e32 v37, v37
	v_add_f32_e32 v38, v14, v182
	v_add_f32_e32 v39, v15, v183
	v_add_f32_e32 v36, 1.0, v36
	v_add_f32_e32 v37, 1.0, v37
	v_mul_f32_e32 v38, 0xbfb8aa3b, v38
	v_mul_f32_e32 v39, 0xbfb8aa3b, v39
	v_rcp_f32_e32 v36, v36
	v_rcp_f32_e32 v37, v37
	v_exp_f32_e32 v38, v38
	v_exp_f32_e32 v39, v39
	v_lshlrev_b32_e32 v106, 16, v70
	v_pk_add_f32 v[46:47], v[36:37], -1.0 op_sel_hi:[1,0]
	v_add_f32_e32 v38, 1.0, v38
	v_add_f32_e32 v39, 1.0, v39
	v_pk_fma_f32 v[46:47], v[184:185], v[46:47], 1.0 op_sel_hi:[1,1,0]
	v_rcp_f32_e32 v38, v38
	v_rcp_f32_e32 v39, v39
	v_pk_mul_f32 v[42:43], v[46:47], v[42:43]
	v_and_b32_e32 v107, 0xffff0000, v70
	v_mul_f32_e32 v46, v42, v106
	v_fmac_f32_e32 v105, v188, v46
	v_lshlrev_b32_e32 v46, 16, v62
	v_and_b32_e32 v47, 0xffff0000, v62
	v_pk_mul_f32 v[36:37], v[36:37], v[46:47]
	v_mul_f32_e32 v46, v43, v107
	v_pk_add_f32 v[80:81], v[38:39], -1.0 op_sel_hi:[1,0]
	v_fmac_f32_e32 v105, v189, v46
	v_lshlrev_b32_e32 v46, 16, v55
	v_and_b32_e32 v47, 0xffff0000, v55
	v_pk_fma_f32 v[80:81], v[186:187], v[80:81], 1.0 op_sel_hi:[1,1,0]
	v_lshlrev_b32_e32 v108, 16, v71
	v_pk_mul_f32 v[46:47], v[80:81], v[46:47]
	v_and_b32_e32 v81, 0xffff0000, v63
	v_mul_f32_e32 v80, v46, v108
	v_fmac_f32_e32 v105, v190, v80
	v_lshlrev_b32_e32 v80, 16, v63
	v_pk_mul_f32 v[38:39], v[38:39], v[80:81]
	v_and_b32_e32 v109, 0xffff0000, v71
	v_cvt_pk_bf16_f32 v42, v42, v43
	v_cvt_pk_bf16_f32 v43, v46, v47
	v_cvt_pk_bf16_f32 v36, v36, v37
	v_cvt_pk_bf16_f32 v37, v38, v39
	v_mul_f32_e32 v80, v47, v109
	ds_write_b64 v41, v[42:43] offset:64
	ds_write_b64 v45, v[36:37] offset:64
	v_fmac_f32_e32 v105, v191, v80
	v_lshlrev_b32_e32 v42, 16, v56
	v_and_b32_e32 v43, 0xffff0000, v56
	v_add_f32_e32 v36, v8, v192
	v_add_f32_e32 v37, v9, v193
	v_mul_f32_e32 v36, 0xbfb8aa3b, v36
	v_mul_f32_e32 v37, 0xbfb8aa3b, v37
	v_exp_f32_e32 v36, v36
	v_exp_f32_e32 v37, v37
	v_lshlrev_b32_e32 v78, 16, v72
	v_and_b32_e32 v96, 0xffff0000, v72
	v_add_f32_e32 v36, 1.0, v36
	v_add_f32_e32 v37, 1.0, v37
	v_rcp_f32_e32 v36, v36
	v_rcp_f32_e32 v37, v37
	v_lshlrev_b32_e32 v104, 16, v73
	v_and_b32_e32 v106, 0xffff0000, v73
	v_mov_b32_e32 v38, v194
	v_mov_b32_e32 v39, v195
	v_mov_b32_e32 v80, v210
	v_mov_b32_e32 v81, v211
	v_mov_b32_e32 v82, v212
	v_mov_b32_e32 v83, v213
	v_mov_b32_e32 v100, v214
	v_mov_b32_e32 v101, v215
	v_mov_b32_e32 v102, v216
	v_mov_b32_e32 v103, v217
	v_cmp_lt_i32_e32 vcc, v207, v202
	v_pk_add_f32 v[46:47], v[36:37], -1.0 op_sel_hi:[1,0]
	s_waitcnt lgkmcnt(1)
	v_pk_fma_f32 v[46:47], v[80:81], v[46:47], 1.0 op_sel_hi:[1,1,0]
	s_nop 0
	v_pk_mul_f32 v[42:43], v[46:47], v[42:43]
	v_and_b32_e32 v47, 0xffff0000, v64
	v_mul_f32_e32 v46, v42, v78
	s_waitcnt lgkmcnt(0)
	v_fmac_f32_e32 v105, v100, v46
	v_lshlrev_b32_e32 v46, 16, v64
	v_pk_mul_f32 v[46:47], v[36:37], v[46:47]
	v_add_f32_e32 v36, v10, v38
	v_add_f32_e32 v37, v11, v39
	v_mul_f32_e32 v36, 0xbfb8aa3b, v36
	v_mul_f32_e32 v37, 0xbfb8aa3b, v37
	v_exp_f32_e32 v36, v36
	v_exp_f32_e32 v37, v37
	v_mul_f32_e32 v38, v43, v96
	v_fmac_f32_e32 v105, v101, v38
	v_add_f32_e32 v36, 1.0, v36
	v_add_f32_e32 v37, 1.0, v37
	v_rcp_f32_e32 v36, v36
	v_rcp_f32_e32 v37, v37
	v_lshlrev_b32_e32 v38, 16, v57
	v_and_b32_e32 v39, 0xffff0000, v57
	v_pk_add_f32 v[80:81], v[36:37], -1.0 op_sel_hi:[1,0]
	s_nop 0
	v_pk_fma_f32 v[80:81], v[82:83], v[80:81], 1.0 op_sel_hi:[1,1,0]
	s_nop 0
	v_pk_mul_f32 v[38:39], v[80:81], v[38:39]
	v_lshlrev_b32_e32 v80, 16, v65
	v_mul_f32_e32 v78, v38, v104
	v_fmac_f32_e32 v105, v102, v78
	v_mul_f32_e32 v78, v39, v106
	v_fmac_f32_e32 v105, v103, v78
	v_cndmask_b32_e32 v78, v200, v207, vcc
	v_lshlrev_b32_e32 v78, 2, v78
	ds_bpermute_b32 v78, v78, v105
	v_and_b32_e32 v81, 0xffff0000, v65
	v_pk_mul_f32 v[80:81], v[36:37], v[80:81]
	v_cvt_pk_bf16_f32 v36, v42, v43
	v_cvt_pk_bf16_f32 v37, v38, v39
	v_cmp_lt_i32_e32 vcc, v208, v202
	ds_write_b64 v41, v[36:37] offset:96
	s_waitcnt lgkmcnt(1)
	v_add_f32_e32 v36, v105, v78
	v_cndmask_b32_e32 v37, v200, v208, vcc
	v_lshlrev_b32_e32 v37, 2, v37
	ds_bpermute_b32 v37, v37, v36
	v_cvt_pk_bf16_f32 v38, v46, v47
	v_cvt_pk_bf16_f32 v39, v80, v81
	v_cmp_gt_u32_e32 vcc, 16, v112
	ds_write_b64 v45, v[38:39] offset:96
	s_and_saveexec_b64 s[44:45], vcc
	s_cbranch_execz .LBB0_547
	s_waitcnt lgkmcnt(1)
	v_add_f32_e32 v38, v36, v37
	v_lshl_add_u64 v[36:37], v[76:77], 0, s[16:17]
	v_readlane_b32 s4, v253, 30
	v_lshlrev_b64 v[36:37], 6, v[36:37]
	v_readlane_b32 s5, v253, 31
	s_lshl_b32 s46, s97, 2
	s_mov_b32 s47, s17
	v_lshl_add_u64 v[36:37], s[4:5], 0, v[36:37]
	s_movk_i32 s4, 0x200
	v_lshl_add_u64 v[36:37], v[36:37], 0, s[46:47]
	global_store_dword v[36:37], v38, off

.LBB0_548:
	s_andn2_b64 vcc, exec, s[44:45]
	s_cbranch_vccnz .LBB0_550
	v_add_u32_e32 v218, 0, v75
	v_add_u32_e32 v219, 0x22500, v218
	ds_read_b128 v[156:159], v219
	ds_read_b128 v[160:163], v219 offset:64
	ds_read_b128 v[164:167], v219 offset:128
	ds_read_b128 v[168:171], v219 offset:192
	v_add_u32_e32 v36, 0, v75
	s_mov_b32 s12, 0xbf1b4598
	s_waitcnt lgkmcnt(0)
	v_add_f32_e32 v20, v20, v156
	v_add_f32_e32 v21, v21, v157
	v_add_f32_e32 v22, v22, v158
	v_add_f32_e32 v23, v23, v159
	v_mul_f32_e32 v20, 0xbfb8aa3b, v20
	v_mul_f32_e32 v21, 0xbfb8aa3b, v21
	v_mul_f32_e32 v22, 0xbfb8aa3b, v22
	v_mul_f32_e32 v23, 0xbfb8aa3b, v23
	v_exp_f32_e32 v20, v20
	v_exp_f32_e32 v21, v21
	v_exp_f32_e32 v22, v22
	v_exp_f32_e32 v23, v23
	v_add_f32_e32 v20, 1.0, v20
	v_add_f32_e32 v21, 1.0, v21
	v_add_f32_e32 v22, 1.0, v22
	v_add_f32_e32 v23, 1.0, v23
	v_rcp_f32_e32 v20, v20
	v_rcp_f32_e32 v21, v21
	v_rcp_f32_e32 v22, v22
	v_rcp_f32_e32 v23, v23
	v_add_u32_e32 v36, 0, v79
	v_pk_mul_f32 v[20:21], v[20:21], s[12:13] op_sel_hi:[1,0]
	v_add_u32_e32 v36, 0x14400, v36
	v_pk_mul_f32 v[22:23], v[22:23], s[12:13] op_sel_hi:[1,0]
	v_cvt_pk_bf16_f32 v20, v20, v21
	v_cvt_pk_bf16_f32 v21, v22, v23
	ds_write_b64 v36, v[20:21]
	v_add_f32_e32 v16, v16, v160
	v_add_f32_e32 v17, v17, v161
	v_add_f32_e32 v18, v18, v162
	v_add_f32_e32 v19, v19, v163
	v_mul_f32_e32 v16, 0xbfb8aa3b, v16
	v_mul_f32_e32 v17, 0xbfb8aa3b, v17
	v_mul_f32_e32 v18, 0xbfb8aa3b, v18
	v_mul_f32_e32 v19, 0xbfb8aa3b, v19
	v_exp_f32_e32 v16, v16
	v_exp_f32_e32 v17, v17
	v_exp_f32_e32 v18, v18
	v_exp_f32_e32 v19, v19
	v_add_f32_e32 v16, 1.0, v16
	v_add_f32_e32 v17, 1.0, v17
	v_add_f32_e32 v18, 1.0, v18
	v_add_f32_e32 v19, 1.0, v19
	v_rcp_f32_e32 v16, v16
	v_rcp_f32_e32 v17, v17
	v_rcp_f32_e32 v18, v18
	v_rcp_f32_e32 v19, v19
	v_pk_mul_f32 v[16:17], v[16:17], s[12:13] op_sel_hi:[1,0]
	s_nop 0
	v_cvt_pk_bf16_f32 v16, v16, v17
	v_pk_mul_f32 v[18:19], v[18:19], s[12:13] op_sel_hi:[1,0]
	s_nop 0
	v_cvt_pk_bf16_f32 v17, v18, v19
	ds_write_b64 v36, v[16:17] offset:32
	v_add_f32_e32 v12, v12, v164
	v_add_f32_e32 v13, v13, v165
	v_add_f32_e32 v14, v14, v166
	v_add_f32_e32 v15, v15, v167
	v_mul_f32_e32 v12, 0xbfb8aa3b, v12
	v_mul_f32_e32 v13, 0xbfb8aa3b, v13
	v_mul_f32_e32 v14, 0xbfb8aa3b, v14
	v_mul_f32_e32 v15, 0xbfb8aa3b, v15
	v_exp_f32_e32 v12, v12
	v_exp_f32_e32 v13, v13
	v_exp_f32_e32 v14, v14
	v_exp_f32_e32 v15, v15
	v_add_f32_e32 v12, 1.0, v12
	v_add_f32_e32 v13, 1.0, v13
	v_add_f32_e32 v14, 1.0, v14
	v_add_f32_e32 v15, 1.0, v15
	v_rcp_f32_e32 v12, v12
	v_rcp_f32_e32 v13, v13
	v_rcp_f32_e32 v14, v14
	v_rcp_f32_e32 v15, v15
	v_pk_mul_f32 v[12:13], v[12:13], s[12:13] op_sel_hi:[1,0]
	s_nop 0
	v_cvt_pk_bf16_f32 v12, v12, v13
	v_pk_mul_f32 v[14:15], v[14:15], s[12:13] op_sel_hi:[1,0]
	s_nop 0
	v_cvt_pk_bf16_f32 v13, v14, v15
	ds_write_b64 v36, v[12:13] offset:64
	v_add_f32_e32 v8, v8, v168
	v_add_f32_e32 v9, v9, v169
	v_add_f32_e32 v10, v10, v170
	v_add_f32_e32 v11, v11, v171
	v_mul_f32_e32 v8, 0xbfb8aa3b, v8
	v_mul_f32_e32 v9, 0xbfb8aa3b, v9
	v_mul_f32_e32 v10, 0xbfb8aa3b, v10
	v_mul_f32_e32 v11, 0xbfb8aa3b, v11
	v_exp_f32_e32 v8, v8
	v_exp_f32_e32 v9, v9
	v_exp_f32_e32 v10, v10
	v_exp_f32_e32 v11, v11
	v_add_f32_e32 v8, 1.0, v8
	v_add_f32_e32 v9, 1.0, v9
	v_add_f32_e32 v10, 1.0, v10
	v_add_f32_e32 v11, 1.0, v11
	v_rcp_f32_e32 v8, v8
	v_rcp_f32_e32 v9, v9
	v_rcp_f32_e32 v10, v10
	v_rcp_f32_e32 v11, v11
	v_pk_mul_f32 v[8:9], v[8:9], s[12:13] op_sel_hi:[1,0]
	s_nop 0
	v_cvt_pk_bf16_f32 v8, v8, v9
	v_pk_mul_f32 v[10:11], v[10:11], s[12:13] op_sel_hi:[1,0]
	s_nop 0
	v_cvt_pk_bf16_f32 v9, v10, v11
	ds_write_b64 v36, v[8:9] offset:96
	v_mov_b32_e32 v12, v168
	v_mov_b32_e32 v13, v169
	v_mov_b32_e32 v14, v170
	v_mov_b32_e32 v15, v171
	v_mov_b32_e32 v16, v164
	v_mov_b32_e32 v17, v165
	v_mov_b32_e32 v18, v166
	v_mov_b32_e32 v19, v167
	v_mov_b32_e32 v20, v160
	v_mov_b32_e32 v21, v161
	v_mov_b32_e32 v22, v162
	v_mov_b32_e32 v23, v163
	v_mov_b32_e32 v37, v157
	v_mov_b32_e32 v38, v158
	v_mov_b32_e32 v39, v159

.LBB0_913:
	s_mul_hi_i32 s3, s4, 0x78787879
	s_lshr_b32 s5, s3, 31
	s_ashr_i32 s3, s3, 7
	s_add_i32 s3, s3, s5
	s_mulk_i32 s3, 0x110
	s_sub_i32 s3, s4, s3
	s_cmp_lt_i32 s3, 16
	v_readlane_b32 s14, v255, 11
	s_cselect_b64 s[6:7], -1, 0
	v_readlane_b32 s15, v255, 12
	s_and_b64 s[6:7], s[14:15], s[6:7]
	s_and_b64 vcc, exec, s[6:7]
	s_cbranch_vccnz .LBB0_912
	v_mov_b32_e32 v104, v96
	v_readlane_b32 s6, v254, 36
	v_ashrrev_i32_e32 v38, 4, v104
	v_and_b32_e32 v105, 15, v104
	v_lshlrev_b32_e32 v34, 2, v38
	v_add_u32_e32 v32, s2, v105
	v_ashrrev_i32_e32 v35, 31, v34
	v_readlane_b32 s7, v254, 37
	v_mov_b64_e32 v[36:37], s[78:79]
	s_movk_i32 s3, 0x480
	v_lshlrev_b32_e32 v38, 3, v38
	v_lshl_add_u64 v[34:35], v[34:35], 0, s[6:7]
	v_mad_i64_i32 v[36:37], s[6:7], v32, s3, v[36:37]
	v_ashrrev_i32_e32 v39, 31, v38
	v_lshl_add_u64 v[36:37], v[38:39], 1, v[36:37]
	s_mov_b64 s[6:7], 0x4869c200
	s_mov_b32 s3, 0x4869c000
	v_lshl_add_u64 v[38:39], v[36:37], 0, s[6:7]
	v_add_co_u32_e32 v36, vcc, s3, v36
	v_ashrrev_i32_e32 v33, 31, v32
	s_nop 0
	v_addc_co_u32_e32 v37, vcc, 0, v37, vcc
	global_load_dwordx4 v[72:75], v[36:37], off offset:512
	global_load_dwordx4 v[68:71], v[38:39], off offset:64
	global_load_dwordx4 v[64:67], v[38:39], off offset:128
	global_load_dwordx4 v[60:63], v[38:39], off offset:192
	global_load_dwordx4 v[56:59], v[38:39], off offset:256
	global_load_dwordx4 v[52:55], v[38:39], off offset:320
	global_load_dwordx4 v[48:51], v[38:39], off offset:384
	global_load_dwordx4 v[44:47], v[38:39], off offset:448
	global_load_dwordx4 v[40:43], v[38:39], off offset:512
	s_nop 0
	global_load_dwordx4 v[36:39], v[38:39], off offset:576
	v_lshlrev_b64 v[76:77], 10, v[32:33]
	v_lshl_add_u64 v[34:35], v[34:35], 0, v[76:77]
	v_readlane_b32 s6, v253, 1
	v_lshlrev_b64 v[92:93], 1, v[34:35]
	v_readlane_b32 s7, v253, 2
	v_lshlrev_b64 v[32:33], 6, v[32:33]
	s_mov_b32 s3, 0x110000
	v_lshl_add_u64 v[34:35], s[6:7], 0, v[92:93]
	v_readlane_b32 s6, v253, 34
	v_readlane_b32 s7, v253, 35
	s_nop 1
	v_lshl_add_u64 v[76:77], s[6:7], 0, v[92:93]
	v_readlane_b32 s6, v253, 26
	v_readlane_b32 s7, v253, 27
	s_nop 1
	v_lshl_add_u64 v[78:79], s[6:7], 0, v[92:93]
	v_readlane_b32 s6, v253, 30
	v_readlane_b32 s7, v253, 31
	global_load_dwordx2 v[94:95], v[34:35], off
	global_load_dwordx2 v[98:99], v[76:77], off
	global_load_dwordx2 v[90:91], v[78:79], off
	global_load_dwordx2 v[82:83], v[34:35], off offset:32
	global_load_dwordx2 v[80:81], v[76:77], off offset:32
	global_load_dwordx2 v[88:89], v[78:79], off offset:32
	global_load_dwordx2 v[112:113], v[34:35], off offset:64
	global_load_dwordx2 v[110:111], v[76:77], off offset:64
	global_load_dwordx2 v[86:87], v[78:79], off offset:64
	global_load_dwordx2 v[102:103], v[34:35], off offset:96
	global_load_dwordx2 v[100:101], v[76:77], off offset:96
	global_load_dwordx2 v[84:85], v[78:79], off offset:96
	v_lshl_add_u64 v[32:33], s[6:7], 0, v[32:33]
	v_readlane_b32 s6, v254, 51
	v_readlane_b32 s7, v254, 52
	s_mov_b32 s7, s17
	s_mov_b32 s14, s6
	v_lshl_add_u64 v[32:33], v[32:33], 0, s[6:7]
	global_load_dword v120, v[32:33], off
	v_add_co_u32_e32 v32, vcc, s3, v32
	v_readlane_b32 s6, v253, 36
	s_nop 0
	v_addc_co_u32_e32 v33, vcc, 0, v33, vcc
	global_load_dword v121, v[32:33], off
	v_and_b32_e32 v32, -16, v104
	v_mul_u32_u24_e32 v33, 0x290, v105
	v_add3_u32 v109, 0, v32, v33
	ds_read_b128 v[126:129], v109
	ds_read_b128 v[130:133], v109 offset:64
	ds_read_b128 v[134:137], v109 offset:21056
	ds_read_b128 v[138:141], v109 offset:31488
	ds_read_b128 v[142:145], v109 offset:128
	ds_read_b128 v[146:149], v109 offset:192
	ds_read_b128 v[150:153], v109 offset:256
	ds_read_b128 v[154:157], v109 offset:320
	ds_read_b128 v[158:161], v109 offset:384
	ds_read_b128 v[162:165], v109 offset:448
	ds_read_b128 v[166:169], v109 offset:512
	ds_read_b128 v[170:173], v109 offset:576
	v_cmp_lt_i32_e32 vcc, v207, v202
	v_readlane_b32 s7, v253, 37
	v_writelane_b32 v254, s14, 51
	s_waitcnt vmcnt(0)
	s_waitcnt lgkmcnt(0)
	v_mfma_f32_16x16x32_bf16 v[32:35], v[126:129], v[72:75], 0
	v_writelane_b32 v254, s15, 52
	v_mfma_f32_16x16x32_bf16 v[32:35], v[130:133], v[68:71], v[32:35]
	v_lshlrev_b32_e32 v104, 16, v98
	v_mfma_f32_16x16x32_bf16 v[32:35], v[142:145], v[64:67], v[32:35]
	v_and_b32_e32 v105, 0xffff0000, v98
	v_lshlrev_b32_e32 v114, 16, v80
	v_mfma_f32_16x16x32_bf16 v[32:35], v[146:149], v[60:63], v[32:35]
	v_and_b32_e32 v115, 0xffff0000, v80
	v_lshlrev_b32_e32 v80, 16, v81
	v_mfma_f32_16x16x32_bf16 v[32:35], v[150:153], v[56:59], v[32:35]
	v_and_b32_e32 v81, 0xffff0000, v81
	v_mfma_f32_16x16x32_bf16 v[32:35], v[154:157], v[52:55], v[32:35]
	v_mfma_f32_16x16x32_bf16 v[32:35], v[158:161], v[48:51], v[32:35]
	v_mfma_f32_16x16x32_bf16 v[32:35], v[162:165], v[44:47], v[32:35]
	v_mfma_f32_16x16x32_bf16 v[32:35], v[166:169], v[40:43], v[32:35]
	v_mfma_f32_16x16x32_bf16 v[32:35], v[170:173], v[36:39], v[32:35]
	v_mov_b32_e32 v76, v170
	v_mov_b32_e32 v77, v171
	v_mov_b32_e32 v78, v172
	v_mov_b32_e32 v79, v173
	v_mov_b32_e32 v116, v134
	v_mov_b32_e32 v117, v135
	v_mov_b32_e32 v118, v136
	v_mov_b32_e32 v119, v137
	v_mov_b32_e32 v122, v138
	v_mov_b32_e32 v123, v139
	v_mov_b32_e32 v124, v140
	v_mov_b32_e32 v125, v141
	ds_read_b128 v[126:129], v109 offset:10560
	ds_read_b128 v[130:133], v109 offset:10496
	ds_read_b128 v[134:137], v109 offset:10624
	ds_read_b128 v[138:141], v109 offset:10688
	ds_read_b128 v[142:145], v109 offset:10752
	ds_read_b128 v[146:149], v109 offset:10816
	ds_read_b128 v[150:153], v109 offset:10880
	ds_read_b128 v[154:157], v109 offset:10944
	ds_read_b128 v[158:161], v109 offset:11008
	ds_read_b128 v[162:165], v109 offset:11072
	v_lshlrev_b32_e32 v76, 16, v94
	v_and_b32_e32 v77, 0xffff0000, v94
	v_lshlrev_b32_e32 v78, 16, v95
	v_and_b32_e32 v79, 0xffff0000, v95
	v_lshlrev_b32_e32 v94, 16, v99
	v_and_b32_e32 v95, 0xffff0000, v99
	v_pk_add_f32 v[94:95], v[78:79], v[94:95]
	v_pk_add_f32 v[98:99], v[76:77], v[104:105]
	v_mov_b32_e32 v79, v95
	v_pk_mov_b32 v[76:77], v[98:99], v[94:95] op_sel:[1,0]
	v_mov_b32_e32 v78, v98
	v_pk_add_f32 v[76:77], v[76:77], v[78:79]
	v_add_f32_e32 v76, v76, v77
	v_add_f32_e32 v108, 0, v76
	s_waitcnt lgkmcnt(0)
	v_mfma_f32_16x16x32_bf16 v[76:79], v[130:133], v[72:75], 0
	v_mfma_f32_16x16x32_bf16 v[76:79], v[126:129], v[68:71], v[76:79]
	v_mfma_f32_16x16x32_bf16 v[76:79], v[134:137], v[64:67], v[76:79]
	v_mfma_f32_16x16x32_bf16 v[76:79], v[138:141], v[60:63], v[76:79]
	v_mfma_f32_16x16x32_bf16 v[76:79], v[142:145], v[56:59], v[76:79]
	v_mfma_f32_16x16x32_bf16 v[76:79], v[146:149], v[52:55], v[76:79]
	v_mfma_f32_16x16x32_bf16 v[76:79], v[150:153], v[48:51], v[76:79]
	v_mfma_f32_16x16x32_bf16 v[76:79], v[154:157], v[44:47], v[76:79]
	v_mfma_f32_16x16x32_bf16 v[76:79], v[158:161], v[40:43], v[76:79]
	v_mfma_f32_16x16x32_bf16 v[76:79], v[162:165], v[36:39], v[76:79]
	v_mov_b32_e32 v104, v162
	v_mov_b32_e32 v105, v163
	v_mov_b32_e32 v106, v164
	v_mov_b32_e32 v107, v165
	ds_read_b128 v[126:129], v109 offset:20992
	ds_read_b128 v[130:133], v109 offset:21120
	ds_read_b128 v[134:137], v109 offset:31552
	ds_read_b128 v[138:141], v109 offset:21184
	ds_read_b128 v[142:145], v109 offset:31616
	ds_read_b128 v[146:149], v109 offset:21248
	ds_read_b128 v[150:153], v109 offset:31680
	ds_read_b128 v[154:157], v109 offset:21312
	ds_read_b128 v[158:161], v109 offset:31744
	v_lshlrev_b32_e32 v106, 16, v82
	v_and_b32_e32 v107, 0xffff0000, v82
	v_lshlrev_b32_e32 v82, 16, v83
	v_and_b32_e32 v83, 0xffff0000, v83
	v_pk_add_f32 v[104:105], v[82:83], v[80:81]
	v_pk_add_f32 v[106:107], v[106:107], v[114:115]
	v_mov_b32_e32 v83, v105
	v_pk_mov_b32 v[80:81], v[106:107], v[104:105] op_sel:[1,0]
	v_mov_b32_e32 v82, v106
	v_pk_add_f32 v[80:81], v[80:81], v[82:83]
	s_nop 0
	v_pk_add_f32 v[114:115], v[80:81], v[80:81] op_sel:[0,1] op_sel_hi:[1,0]
	s_waitcnt lgkmcnt(0)
	v_mfma_f32_16x16x32_bf16 v[80:83], v[126:129], v[72:75], 0
	v_mfma_f32_16x16x32_bf16 v[80:83], v[116:119], v[68:71], v[80:83]
	v_mfma_f32_16x16x32_bf16 v[72:75], v[122:125], v[72:75], 0
	v_mfma_f32_16x16x32_bf16 v[80:83], v[130:133], v[64:67], v[80:83]
	v_mfma_f32_16x16x32_bf16 v[68:71], v[134:137], v[68:71], v[72:75]
	s_nop 2
	v_mfma_f32_16x16x32_bf16 v[80:83], v[138:141], v[60:63], v[80:83]
	v_mfma_f32_16x16x32_bf16 v[64:67], v[142:145], v[64:67], v[68:71]
	s_nop 2
	v_mfma_f32_16x16x32_bf16 v[80:83], v[146:149], v[56:59], v[80:83]
	v_mfma_f32_16x16x32_bf16 v[60:63], v[150:153], v[60:63], v[64:67]
	s_nop 2
	v_mfma_f32_16x16x32_bf16 v[80:83], v[154:157], v[52:55], v[80:83]
	v_mov_b32_e32 v64, v158
	v_mov_b32_e32 v65, v159
	v_mov_b32_e32 v66, v160
	v_mov_b32_e32 v67, v161
	v_mov_b32_e32 v68, v150
	v_mov_b32_e32 v69, v151
	v_mov_b32_e32 v70, v152
	v_mov_b32_e32 v71, v153
	v_mov_b32_e32 v72, v142
	v_mov_b32_e32 v73, v143
	v_mov_b32_e32 v74, v144
	v_mov_b32_e32 v75, v145
	v_mov_b32_e32 v116, v154
	v_mov_b32_e32 v117, v155
	v_mov_b32_e32 v118, v156
	v_mov_b32_e32 v119, v157
	v_mov_b32_e32 v122, v134
	v_mov_b32_e32 v123, v135
	v_mov_b32_e32 v124, v136
	v_mov_b32_e32 v125, v137
	ds_read_b128 v[126:129], v109 offset:21376
	ds_read_b128 v[130:133], v109 offset:31808
	ds_read_b128 v[134:137], v109 offset:21440
	ds_read_b128 v[138:141], v109 offset:31872
	ds_read_b128 v[142:145], v109 offset:21504
	ds_read_b128 v[146:149], v109 offset:31936
	ds_read_b128 v[150:153], v109 offset:21568
	ds_read_b128 v[154:157], v109 offset:32000
	ds_read_b128 v[158:161], v109 offset:32064
	v_mfma_f32_16x16x32_bf16 v[56:59], v[64:67], v[56:59], v[60:63]
	s_nop 2
	s_waitcnt lgkmcnt(0)
	v_mfma_f32_16x16x32_bf16 v[80:83], v[126:129], v[48:51], v[80:83]
	v_mfma_f32_16x16x32_bf16 v[52:55], v[130:133], v[52:55], v[56:59]
	s_nop 2
	v_mfma_f32_16x16x32_bf16 v[80:83], v[134:137], v[44:47], v[80:83]
	v_mfma_f32_16x16x32_bf16 v[48:51], v[138:141], v[48:51], v[52:55]
	s_nop 2
	v_lshlrev_b32_e32 v56, 16, v91
	v_and_b32_e32 v57, 0xffff0000, v91
	v_mfma_f32_16x16x32_bf16 v[80:83], v[142:145], v[40:43], v[80:83]
	v_mfma_f32_16x16x32_bf16 v[44:47], v[146:149], v[44:47], v[48:51]
	v_and_b32_e32 v55, 0xffff0000, v90
	s_nop 1
	v_mfma_f32_16x16x32_bf16 v[40:43], v[154:157], v[40:43], v[44:47]
	s_nop 2
	v_mfma_f32_16x16x32_bf16 v[80:83], v[150:153], v[36:39], v[80:83]
	v_lshlrev_b32_e32 v116, 16, v112
	v_and_b32_e32 v117, 0xffff0000, v112
	v_lshlrev_b32_e32 v112, 16, v113
	v_and_b32_e32 v113, 0xffff0000, v113
	v_lshlrev_b32_e32 v118, 16, v110
	v_and_b32_e32 v119, 0xffff0000, v110
	v_lshlrev_b32_e32 v110, 16, v111
	v_and_b32_e32 v111, 0xffff0000, v111
	v_mfma_f32_16x16x32_bf16 v[36:39], v[158:161], v[36:39], v[40:43]
	v_mov_b32_e32 v44, v158
	v_mov_b32_e32 v45, v159
	v_mov_b32_e32 v46, v160
	v_mov_b32_e32 v47, v161
	v_mov_b32_e32 v48, v154
	v_mov_b32_e32 v49, v155
	v_mov_b32_e32 v50, v156
	v_mov_b32_e32 v51, v157
	v_mov_b32_e32 v52, v146
	v_mov_b32_e32 v53, v147
	v_mov_b32_e32 v54, v148
	v_mov_b32_e32 v58, v140
	v_mov_b32_e32 v59, v141
	v_mov_b32_e32 v60, v130
	v_mov_b32_e32 v61, v131
	v_mov_b32_e32 v62, v132
	v_mov_b32_e32 v63, v133
	v_lshlrev_b32_e32 v44, 16, v100
	v_and_b32_e32 v45, 0xffff0000, v100
	v_lshlrev_b32_e32 v46, 16, v101
	v_lshlrev_b32_e32 v42, 16, v102
	v_and_b32_e32 v43, 0xffff0000, v102
	v_lshlrev_b32_e32 v40, 16, v103
	v_and_b32_e32 v41, 0xffff0000, v103
	v_and_b32_e32 v47, 0xffff0000, v101
	v_pk_add_f32 v[110:111], v[112:113], v[110:111]
	v_pk_add_f32 v[112:113], v[116:117], v[118:119]
	v_pk_add_f32 v[40:41], v[40:41], v[46:47]
	v_pk_add_f32 v[42:43], v[42:43], v[44:45]
	v_add_f32_e32 v116, v112, v113
	v_add_f32_e32 v118, v110, v111
	v_mov_b32_e32 v109, v42
	v_mov_b32_e32 v115, v43
	v_mov_b32_e32 v117, v40
	v_mov_b32_e32 v119, v41
	v_pk_add_f32 v[44:45], v[108:109], v[114:115]
	v_pk_add_f32 v[46:47], v[116:117], v[118:119]
	s_nop 0
	v_pk_add_f32 v[44:45], v[44:45], v[46:47]
	s_nop 0
	v_add_f32_e32 v44, v44, v45
	v_cndmask_b32_e32 v45, v200, v207, vcc
	v_lshlrev_b32_e32 v52, 2, v45
	ds_bpermute_b32 v45, v52, v44
	v_cmp_lt_i32_e32 vcc, v208, v202
	s_waitcnt lgkmcnt(0)
	v_add_f32_e32 v44, v44, v45
	v_cndmask_b32_e32 v45, v200, v208, vcc
	v_lshlrev_b32_e32 v53, 2, v45
	ds_bpermute_b32 v45, v53, v44
	s_waitcnt lgkmcnt(0)
	v_add_f32_e32 v54, v44, v45
	v_fmamk_f32 v99, v54, 0xbc800000, v99
	v_fmac_f32_e32 v98, 0xbc800000, v54
	v_fmamk_f32 v95, v54, 0xbc800000, v95
	v_fmac_f32_e32 v94, 0xbc800000, v54
	v_pk_mul_f32 v[44:45], v[94:95], v[94:95]
	v_pk_mul_f32 v[46:47], v[98:99], v[98:99]
	v_fmamk_f32 v107, v54, 0xbc800000, v107
	v_pk_mov_b32 v[48:49], v[46:47], v[44:45] op_sel:[1,0]
	v_mov_b32_e32 v47, v45
	v_pk_add_f32 v[44:45], v[48:49], v[46:47]
	v_fmac_f32_e32 v106, 0xbc800000, v54
	v_fmamk_f32 v105, v54, 0xbc800000, v105
	v_fmac_f32_e32 v104, 0xbc800000, v54
	v_pk_add_f32 v[44:45], v[44:45], v[44:45] op_sel_hi:[0,1]
	v_pk_mul_f32 v[46:47], v[104:105], v[104:105]
	v_pk_mul_f32 v[48:49], v[106:107], v[106:107]
	v_fmac_f32_e32 v112, 0xbc800000, v54
	v_pk_mov_b32 v[50:51], v[48:49], v[46:47] op_sel:[1,0]
	v_mov_b32_e32 v49, v47
	v_fmamk_f32 v113, v54, 0xbc800000, v113
	v_fmac_f32_e32 v110, 0xbc800000, v54
	v_mul_f32_e32 v44, v112, v112
	v_pk_add_f32 v[46:47], v[50:51], v[48:49]
	v_fmamk_f32 v111, v54, 0xbc800000, v111
	v_pk_fma_f32 v[48:49], v[112:113], v[112:113], v[44:45] op_sel_hi:[1,1,0]
	v_mul_f32_e32 v44, v110, v110
	v_pk_add_f32 v[46:47], v[46:47], v[46:47] op_sel_hi:[0,1]
	v_pk_fma_f32 v[50:51], v[110:111], v[110:111], v[44:45] op_sel_hi:[1,1,0]
	v_fmamk_f32 v41, v54, 0xbc800000, v41
	v_fmac_f32_e32 v40, 0xbc800000, v54
	v_fmamk_f32 v43, v54, 0xbc800000, v43
	v_fmac_f32_e32 v42, 0xbc800000, v54
	v_mul_f32_e32 v48, v42, v42
	v_mul_f32_e32 v50, v43, v43
	v_mul_f32_e32 v44, v40, v40
	v_mul_f32_e32 v46, v41, v41
	v_pk_add_f32 v[48:49], v[48:49], v[50:51]
	v_pk_add_f32 v[44:45], v[44:45], v[46:47]
	v_lshlrev_b32_e32 v54, 16, v90
	v_pk_add_f32 v[44:45], v[48:49], v[44:45]
	v_lshl_add_u64 v[48:49], s[6:7], 0, v[92:93]
	v_add_f32_e32 v45, v44, v45
	ds_bpermute_b32 v46, v52, v45
	v_add_f32_e32 v44, v120, v121
	s_waitcnt lgkmcnt(0)
	v_add_f32_e32 v45, v45, v46
	ds_bpermute_b32 v46, v53, v45
	s_waitcnt lgkmcnt(0)
	v_add_f32_e32 v45, v45, v46
	v_mov_b32_e32 v46, 0x3a27c5ac
	v_fmamk_f32 v45, v45, 0x3c800000, v46
	v_cmp_gt_f32_e32 vcc, s35, v45
	v_mul_f32_e32 v46, 0x4b800000, v45
	s_nop 0
	v_cndmask_b32_e32 v45, v45, v46, vcc
	v_rsq_f32_e32 v45, v45
	s_nop 0
	v_mul_f32_e32 v46, 0x45800000, v45
	v_cndmask_b32_e32 v46, v45, v46, vcc
	v_pk_mul_f32 v[50:51], v[98:99], v[46:47] op_sel_hi:[1,0]
	v_pk_mul_f32 v[52:53], v[94:95], v[46:47] op_sel_hi:[1,0]
	v_pk_fma_f32 v[50:51], v[0:1], v[50:51], v[4:5]
	v_pk_fma_f32 v[52:53], v[2:3], v[52:53], v[6:7]
	v_pk_fma_f32 v[50:51], v[44:45], v[54:55], v[50:51] op_sel_hi:[0,1,1]
	v_pk_fma_f32 v[52:53], v[44:45], v[56:57], v[52:53] op_sel_hi:[0,1,1]
	v_pk_mul_f32 v[34:35], v[34:35], v[52:53]
	v_pk_mul_f32 v[32:33], v[32:33], v[50:51]
	v_lshlrev_b32_e32 v50, 16, v88
	v_cvt_pk_bf16_f32 v32, v32, v33
	v_cvt_pk_bf16_f32 v33, v34, v35
	global_store_dwordx2 v[48:49], v[32:33], off
	v_pk_mul_f32 v[32:33], v[106:107], v[46:47] op_sel_hi:[1,0]
	v_pk_mul_f32 v[34:35], v[104:105], v[46:47] op_sel_hi:[1,0]
	v_pk_fma_f32 v[32:33], v[8:9], v[32:33], v[12:13]
	v_pk_fma_f32 v[34:35], v[10:11], v[34:35], v[14:15]
	v_and_b32_e32 v51, 0xffff0000, v88
	v_lshlrev_b32_e32 v52, 16, v89
	v_and_b32_e32 v53, 0xffff0000, v89
	v_pk_fma_f32 v[32:33], v[44:45], v[50:51], v[32:33] op_sel_hi:[0,1,1]
	v_pk_fma_f32 v[34:35], v[44:45], v[52:53], v[34:35] op_sel_hi:[0,1,1]
	v_pk_mul_f32 v[34:35], v[78:79], v[34:35]
	v_pk_mul_f32 v[32:33], v[76:77], v[32:33]
	v_lshlrev_b32_e32 v50, 16, v86
	v_cvt_pk_bf16_f32 v32, v32, v33
	v_cvt_pk_bf16_f32 v33, v34, v35
	global_store_dwordx2 v[48:49], v[32:33], off offset:32
	v_pk_mul_f32 v[32:33], v[112:113], v[46:47] op_sel_hi:[1,0]
	v_pk_mul_f32 v[34:35], v[110:111], v[46:47] op_sel_hi:[1,0]
	v_pk_fma_f32 v[32:33], v[16:17], v[32:33], v[20:21]
	v_pk_fma_f32 v[34:35], v[18:19], v[34:35], v[22:23]
	v_and_b32_e32 v51, 0xffff0000, v86
	v_lshlrev_b32_e32 v52, 16, v87
	v_and_b32_e32 v53, 0xffff0000, v87
	v_pk_fma_f32 v[32:33], v[44:45], v[50:51], v[32:33] op_sel_hi:[0,1,1]
	v_pk_fma_f32 v[34:35], v[44:45], v[52:53], v[34:35] op_sel_hi:[0,1,1]
	v_pk_mul_f32 v[34:35], v[82:83], v[34:35]
	v_pk_mul_f32 v[32:33], v[80:81], v[32:33]
	s_nop 0
	v_cvt_pk_bf16_f32 v32, v32, v33
	v_cvt_pk_bf16_f32 v33, v34, v35
	global_store_dwordx2 v[48:49], v[32:33], off offset:64
	v_pk_mul_f32 v[32:33], v[42:43], v[46:47] op_sel_hi:[1,0]
	v_pk_mul_f32 v[34:35], v[40:41], v[46:47] op_sel_hi:[1,0]
	v_pk_fma_f32 v[32:33], v[24:25], v[32:33], v[28:29]
	v_pk_fma_f32 v[34:35], v[26:27], v[34:35], v[30:31]
	v_lshlrev_b32_e32 v40, 16, v84
	v_and_b32_e32 v41, 0xffff0000, v84
	v_lshlrev_b32_e32 v42, 16, v85
	v_and_b32_e32 v43, 0xffff0000, v85
	v_pk_fma_f32 v[32:33], v[44:45], v[40:41], v[32:33] op_sel_hi:[0,1,1]
	v_pk_fma_f32 v[34:35], v[44:45], v[42:43], v[34:35] op_sel_hi:[0,1,1]
	v_pk_mul_f32 v[34:35], v[38:39], v[34:35]
	v_pk_mul_f32 v[32:33], v[36:37], v[32:33]
	s_nop 0
	v_cvt_pk_bf16_f32 v32, v32, v33
	v_cvt_pk_bf16_f32 v33, v34, v35
	global_store_dwordx2 v[48:49], v[32:33], off offset:96
	s_branch .LBB0_912
